# layer-1 expert-weight staging moved into the attention main loop (6 waves per CU, 1 KiB slab per step, LDS-transposed, 64-byte row stores); output projection runs one unit on every CU
# baseline (speedup 1.0000x reference)
; #define LAS __attribute__((address_space(3)))
; #define WAIT_BAR(N) asm volatile("s_waitcnt vmcnt(" #N ") lgkmcnt(0)\n\ts_barrier" ::: "memory")
;     __device__ __forceinline__ const float* x() const { return (const float*)ld(0); }
; template <int THRL> ...
;   const int tid = threadIdx.x, lane = tid & 63, r32 = lane & 31, hi = lane >> 5; const int wid = __builtin_amdgcn_readfirstlane(tid >> 6);
;   const int comp = wid >> 2, wq = wid & 3;
;   if (wid >= 4) __builtin_amdgcn_s_setprio(1);
;   const bf16_t* Qw = Q + (size_t)(CTXL + qb * 128 + wq * QBLK) * DMK + head * 128 + comp * 64;
;   const bf16_t* Kh = K + head * 128; const bf16_t* Vh = V + head * 128;
;   const unsigned lds0 = (unsigned)(uintptr_t)shm;
;   LAS float* wsf = (LAS float*)(shm + LDS_WS) + wid * 64;
;   const unsigned kvoff = (unsigned)(lane * DMK + wid * 8) * 2u;
;   const unsigned vvoff = (unsigned)((16 * (wid & 3) + (lane >> 2)) * DMK + (wid >> 2) * 32 + (lane & 3) * 8) * 2u;
;   const unsigned kdst = lds0 + LDS_K + wid * 1024, vdst = lds0 + LDS_V + wid * 1024;
;     ...
;   const int vb0 = (int)(lds0 + LDS_V) + ((lane >> 4) & 1) * 32 + (lane & 3) * 8 + (4 * hi + ((lane & 15) >> 2)) * 64;
;   bf16x8 kf[8];
;   const lds_cptr shm3 = (lds_cptr)shm; const lds_cptr kp0 = shm3 + LDS_K + comp * 8192 + hi * 1024 + r32 * 16;
;   const lds_cptr vp0 = shm3 + LDS_V + ((lane >> 4) & 1) * 32 + (lane & 3) * 8 + (4 * hi + ((lane & 15) >> 2)) * 64;
;   DMA_K(0, 0); DMA_V(0, 0); DMA_K(1, SLOTB);
;   bf16x8 qr[4];
; #pragma unroll
;   for (int d0 = 0; d0 < 4; ++d0) qr[d0] = *reinterpret_cast<const bf16x8*>(&Qw[(long)r32 * DMK + d0 * 16 + hi * 8]);
;   float mhat = 0.f, l_reg = 0.f; f32x16 o[4]; o[0] = f32x16{}; o[1] = f32x16{}; o[2] = f32x16{}; o[3] = f32x16{}; f32x16 negm = f32x16{}; asm volatile("" : "+v"(negm));
;   bool resc = false;
;     ...
;   f32x16 pA0, pA1, pB0, pB1;
;   int sl_prev = 0, sl_cur = 0, sl_next = SLOTB;
;     ...
;   DMA_K(2, 2 * SLOTB);
;   WAIT_BAR(6);
;   qkt(pA0, pA1, kp0, qr, negm); asm volatile("s_nop 15\n\ts_nop 7" : "+v"(pA0), "+v"(pA1));
;   const lds_cptr qp = shm3 + LDS_Q + wid * 4096 + lane * 16;
; #pragma unroll
;   for (int d0 = 0; d0 < 4; ++d0) *(LAS bf16x8*)(shm + LDS_Q + wid * 4096 + lane * 16 + d0 * 1024) = qr[d0];
;   START(pA0, pA1);
; #pragma unroll
;   for (int r = 0; r < 16; ++r) pA1[r] = __builtin_amdgcn_exp2f(pA1[r]);
.LBB0_527:
	s_lshl_b32 s0, s28, 1
	s_and_b32 s0, s0, 0x700
	s_add_u32 s33, s26, s0
	s_addc_u32 s53, s27, 0
	s_bfe_u32 s41, s39, 0x20006
	s_lshl_b32 s0, s36, 4
	s_and_b32 s37, s0, 0xffffff80
	s_lshl_b32 s0, s41, 5
	s_or_b32 s0, s37, s0
	s_addk_i32 s0, 0x100
	s_ashr_i32 s1, s0, 31
	s_lshr_b32 s40, s39, 6
	s_lshr_b32 s42, s39, 8
	s_lshl_b64 s[0:1], s[0:1], 11
	s_add_u32 s0, s5, s0
	s_addc_u32 s1, s17, s1
	s_lshl_b32 s2, s36, 7
	s_and_b32 s14, s2, 0x380
	s_lshl_b32 s8, s14, 1
	s_add_u32 s0, s0, s8
	s_addc_u32 s1, s1, 0
	s_lshl_b32 s43, s42, 6
	s_lshl_b32 s2, s42, 7
	s_add_u32 s2, s0, s2
	s_addc_u32 s3, s1, 0
	s_add_u32 s20, s22, s8
	s_addc_u32 s21, s23, 0
	s_add_u32 s8, s24, s8
	s_addc_u32 s9, s25, 0
	s_lshl_b32 s0, s41, 15
	s_add_i32 s0, s0, s43
	v_add_u32_e32 v235, s0, v219
	s_lshl_b32 s0, s40, 10
	s_add_i32 s49, s0, 0
	s_and_b32 s1, s39, 0x3fffffc0
	s_lshl_b32 s38, s40, 4
	s_add_i32 s46, s49, 0xc000
	s_add_u32 s44, s20, 0x80
	v_add_u32_e32 v237, s38, v218
	s_mov_b32 s0, m0
	s_mov_b32 m0, s49
	s_nop 0
	global_load_lds_dwordx4 v237, s[20:21] offset:0
	s_mov_b32 m0, s0
	s_addc_u32 s45, s21, 0
	s_add_i32 s54, s49, 0x2000
	s_mov_b32 s0, m0
	s_mov_b32 m0, s54
	s_nop 0
	global_load_lds_dwordx4 v237, s[44:45] offset:0
	s_mov_b32 m0, s0
	s_add_u32 s50, s8, 0x80
	s_mov_b32 s0, m0
	s_mov_b32 m0, s46
	s_nop 0
	global_load_lds_dwordx4 v235, s[8:9] offset:0
	s_mov_b32 m0, s0
	s_addc_u32 s51, s9, 0
	s_add_i32 s45, s49, 0xe000
	s_mov_b32 s0, m0
	s_mov_b32 m0, s45
	s_nop 0
	global_load_lds_dwordx4 v235, s[50:51] offset:0
	s_mov_b32 m0, s0
	s_add_u32 s50, s20, 0x20000
	s_addc_u32 s51, s21, 0
	s_add_i32 s52, s49, 0x4000
	s_mov_b32 s0, m0
	s_mov_b32 m0, s52
	s_nop 0
	global_load_lds_dwordx4 v237, s[50:51] offset:0
	s_mov_b32 m0, s0
	s_add_u32 s56, s20, 0x20080
	s_addc_u32 s57, s21, 0
	s_add_i32 s51, s49, 0x6000
	s_mov_b32 s0, m0
	s_mov_b32 m0, s51
	s_nop 0
	global_load_lds_dwordx4 v237, s[56:57] offset:0
	s_mov_b32 m0, s0
	global_load_dwordx4 v[66:69], v229, s[2:3]
	global_load_dwordx4 v[70:73], v229, s[2:3] offset:32
	global_load_dwordx4 v[74:77], v229, s[2:3] offset:64
	global_load_dwordx4 v[78:81], v229, s[2:3] offset:96
	v_mov_b64_e32 v[48:49], v[32:33]
	s_add_u32 s2, s20, 0x40000
	v_mov_b64_e32 v[46:47], v[30:31]
	v_mov_b64_e32 v[44:45], v[28:29]
	v_mov_b64_e32 v[42:43], v[26:27]
	v_mov_b64_e32 v[40:41], v[24:25]
	v_mov_b64_e32 v[38:39], v[22:23]
	v_mov_b64_e32 v[36:37], v[20:21]
	v_mov_b64_e32 v[34:35], v[18:19]
	s_addc_u32 s3, s21, 0
	s_add_i32 s48, s49, 0x8000
	s_mov_b32 s0, m0
	s_mov_b32 m0, s48
	s_nop 0
	global_load_lds_dwordx4 v237, s[2:3] offset:0
	s_mov_b32 m0, s0
	s_add_u32 s2, s20, 0x40080
	s_addc_u32 s3, s21, 0
	s_add_i32 s47, s49, 0xa000
	s_mov_b32 s0, m0
	s_mov_b32 m0, s47
	s_nop 0
	global_load_lds_dwordx4 v237, s[2:3] offset:0
	s_mov_b32 m0, s0
	v_lshl_add_u32 v236, s42, 13, v221
	s_waitcnt vmcnt(6) lgkmcnt(0)
	s_barrier
	ds_read_b128 v[4:7], v236
	s_lshl_b32 s2, s40, 12
	v_add_u32_e32 v233, s2, v222
	s_lshl_b32 s1, s1, 2
	s_add_i32 s50, s1, 0
	s_add_i32 s50, s50, 0x18000
	s_add_u32 s2, s20, 0x60000
	s_addc_u32 s3, s21, 0
	v_mov_b32_e32 v3, v2
	v_mov_b32_e32 v12, v2
	v_mov_b32_e32 v13, v2
	s_movk_i32 s57, 0x4000
	s_mov_b32 s0, 0
	s_mov_b32 s55, 0x8000
	v_lshl_add_u32 v232, v217, 2, s50
	v_mov_b32_e32 v238, 0
	s_mov_b32 s56, -1
	s_waitcnt vmcnt(3) lgkmcnt(0)
	v_mfma_f32_32x32x16_bf16 v[50:65], v[4:7], v[66:69], v[34:49]
	ds_read_b128 v[4:7], v236 offset:512
	s_waitcnt lgkmcnt(0)
	v_mfma_f32_32x32x16_bf16 v[34:49], v[4:7], v[66:69], v[34:49]
	ds_read_b128 v[4:7], v236 offset:2048
	s_waitcnt vmcnt(2) lgkmcnt(0)
	v_mfma_f32_32x32x16_bf16 v[50:65], v[4:7], v[70:73], v[50:65]
	ds_read_b128 v[4:7], v236 offset:2560
	s_waitcnt lgkmcnt(0)
	v_mfma_f32_32x32x16_bf16 v[34:49], v[4:7], v[70:73], v[34:49]
	ds_read_b128 v[4:7], v236 offset:4096
	ds_read_b128 v[8:11], v236 offset:4608
	ds_read_b128 v[82:85], v236 offset:6656
	ds_read_b128 v[14:17], v236 offset:6144
	s_waitcnt vmcnt(1) lgkmcnt(3)
	v_mfma_f32_32x32x16_bf16 v[50:65], v[4:7], v[74:77], v[50:65]
	v_mov_b32_e32 v4, v2
	v_mov_b32_e32 v5, v2
	v_mov_b32_e32 v6, v2
	v_mov_b32_e32 v7, v2
	s_waitcnt lgkmcnt(2)
	v_mfma_f32_32x32x16_bf16 v[34:49], v[8:11], v[74:77], v[34:49]
	v_mov_b32_e32 v8, v2
	v_mov_b32_e32 v9, v2
	v_mov_b32_e32 v10, v2
	v_mov_b32_e32 v11, v2
	s_waitcnt vmcnt(0) lgkmcnt(0)
	v_mfma_f32_32x32x16_bf16 v[50:65], v[14:17], v[78:81], v[50:65]
	v_mov_b32_e32 v16, v2
	v_mov_b32_e32 v17, v2
	v_mov_b32_e32 v14, v2
	v_mov_b32_e32 v15, v2
	v_mfma_f32_32x32x16_bf16 v[34:49], v[82:85], v[78:81], v[34:49]
	s_nop 15
	s_nop 7
	ds_write_b128 v233, v[66:69]
	ds_write_b128 v233, v[70:73] offset:1024
	ds_write_b128 v233, v[74:77] offset:2048
	ds_write_b128 v233, v[78:81] offset:3072
	v_max3_f32 v66, v50, v51, v34
	v_max3_f32 v67, v52, v53, v35
	v_mov_b64_e32 v[96:97], v[16:17]
	v_max3_f32 v66, v66, v36, v37
	v_max3_f32 v67, v67, v56, v57
	v_mov_b64_e32 v[94:95], v[14:15]
	v_max3_f32 v66, v66, v54, v55
	v_max3_f32 v67, v67, v40, v41
	v_mov_b64_e32 v[92:93], v[12:13]
	v_max3_f32 v66, v66, v38, v39
	v_max3_f32 v67, v67, v60, v61
	v_mov_b64_e32 v[90:91], v[10:11]
	v_max3_f32 v66, v66, v58, v59
	v_max3_f32 v67, v67, v44, v45
	v_mov_b64_e32 v[88:89], v[8:9]
	v_max3_f32 v66, v66, v42, v43
	v_max3_f32 v67, v67, v64, v65
	v_mov_b64_e32 v[86:87], v[6:7]
	v_max3_f32 v66, v66, v62, v63
	v_max3_f32 v67, v67, v48, v49
	v_mov_b64_e32 v[84:85], v[4:5]
	v_max3_f32 v66, v66, v46, v47
	v_mov_b64_e32 v[82:83], v[2:3]
	v_max_f32_e32 v66, v66, v67
	s_nop 0
	v_mov_b32_e32 v67, v66
	s_nop 1
	v_permlane32_swap_b32_e32 v66, v67
	v_max_f32_e32 v66, v66, v67
	s_nop 0
	v_add_f32_e32 v234, v2, v66
	v_sub_f32_e32 v50, v50, v66
	v_sub_f32_e32 v34, v34, v66
	v_sub_f32_e32 v51, v51, v66
	v_sub_f32_e32 v35, v35, v66
	v_sub_f32_e32 v52, v52, v66
	s_nop 0
	v_xor_b32_e32 v98, 0x80000000, v234
	v_mov_b32_e32 v99, v98
	v_mov_b32_e32 v100, v98
	v_mov_b32_e32 v101, v98
	v_mov_b32_e32 v102, v98
	v_mov_b32_e32 v103, v98
	v_mov_b32_e32 v104, v98
	v_mov_b32_e32 v105, v98
	v_mov_b32_e32 v106, v98
	v_mov_b32_e32 v107, v98
	v_mov_b32_e32 v108, v98
	v_mov_b32_e32 v109, v98
	v_mov_b32_e32 v110, v98
	v_mov_b32_e32 v111, v98
	v_mov_b32_e32 v112, v98
	v_mov_b32_e32 v113, v98
	s_waitcnt vmcnt(0) lgkmcnt(0)
	s_barrier
; #define LAS __attribute__((address_space(3)))
; #define WAIT_BAR(N) asm volatile("s_waitcnt vmcnt(" #N ") lgkmcnt(0)\n\ts_barrier" ::: "memory")
; #define DMA_K(t, slot) do { const bf16_t* sb_ = Kh + (long)(t) * KVBLK * DMK; glds16<0>(sb_, kvoff, (unsigned)__builtin_amdgcn_readfirstlane(kdst + (slot))); glds16<0>(sb_ + 64, kvoff, (unsigned)__builtin_amdgcn_readfirstlane(kdst + 8192 + (slot))); } while (0)
; #define DMA_V(t, slot) do { const bf16_t* sb_ = Vh + (long)(t) * KVBLK * DMK; glds16<0>(sb_, vvoff, (unsigned)__builtin_amdgcn_readfirstlane(vdst + (slot))); glds16<0>(sb_ + 64, vvoff, (unsigned)__builtin_amdgcn_readfirstlane(vdst + 8192 + (slot))); } while (0)
; #define ROT() do { sl_prev = sl_cur; sl_cur = sl_next; sl_next = (sl_next == (NSLOT - 1) * SLOTB) ? 0 : sl_next + SLOTB; } while (0)
;     __device__ __forceinline__ const float* w_gate() const { return (const float*)ld(21); }
; template <int THRL> ...
;     ...
;   for (int r = 0; r < 16; ++r) pA1[r] = __builtin_amdgcn_exp2f(pA1[r]);
;   WAIT_BAR(0);
;   DMA_K(3, 0); DMA_V(1, SLOTB);
;   ROT();
;   kload8(kf, kp0 + sl_cur);
;   WAIT_BAR(4);
; __device__ __forceinline__ void convert_moe_items(const Ctx& a, int layer, LAS unsigned char* lds, int it0, int it1, int widx, int nw, int wave, int lane) {
;     LAS float* scr = (LAS float*)(lds + wave * 16384);
;     bf16_t* WGU = (bf16_t*)(a.ws() + WS_WGU + (size_t)layer * WGU_BYTES); bf16_t* WD = (bf16_t*)(a.ws() + WS_WD + (size_t)layer * WD_BYTES);
;     constexpr int I_G = (DM / 64) * (FE / 32), I_D = (FE / 64) * (DM / 32);
;     constexpr int PER_E = 2 * I_G + I_D;
;     const float *wg = a.w_gate(), *wu = a.w_up(), *wd = a.w_down();
;     auto decode = [&](int it) { CvtItem d; const int e = it / PER_E; int r = it % PER_E; const size_t eo = ((size_t)layer * NE + e) * (size_t)DM * FE;
;         if (r < I_G)          { d.src = wg + eo; d.dst = WGU; d.N = FE; d.K = DM; d.row_off = e * 2048; d.ilv = 1; }
;         else if (r < 2 * I_G) { r -= I_G; d.src = wu + eo; d.dst = WGU; d.N = FE; d.K = DM; d.row_off = e * 2048 + 128; d.ilv = 1; }
;         else                  { r -= 2 * I_G; d.src = wd + eo; d.dst = WD; d.N = DM; d.K = FE; d.row_off = e * 2048; d.ilv = 0; }
;         const int nblk = d.N / 32; d.k0 = 64 * (r / nblk); d.n0 = 32 * (r % nblk); return d; };
;     int it = it0 + widx;
	s_mov_b32 s1, m0
	s_mov_b32 m0, s49
	s_nop 0
	global_load_lds_dwordx4 v237, s[2:3] offset:0
	s_mov_b32 m0, s1
	s_add_u32 s2, s20, 0x60080
	s_addc_u32 s3, s21, 0
	s_mov_b32 s1, m0
	s_mov_b32 m0, s54
	s_nop 0
	global_load_lds_dwordx4 v237, s[2:3] offset:0
	s_mov_b32 m0, s1
	s_add_u32 s2, s8, 0x20000
	s_addc_u32 s3, s9, 0
	s_add_i32 s44, s49, 0x10000
	s_mov_b32 s1, m0
	s_mov_b32 m0, s44
	s_nop 0
	global_load_lds_dwordx4 v235, s[2:3] offset:0
	s_mov_b32 m0, s1
	s_add_u32 s2, s8, 0x20080
	s_addc_u32 s3, s9, 0
	s_add_i32 s43, s49, 0x12000
	s_mov_b32 s1, m0
	s_mov_b32 m0, s43
	s_nop 0
	global_load_lds_dwordx4 v235, s[2:3] offset:0
	s_mov_b32 m0, s1
	ds_read_b128 v[146:149], v236 offset:16384
	ds_read_b128 v[202:205], v236 offset:16896
	ds_read_b128 v[206:209], v236 offset:18432
	ds_read_b128 v[190:193], v236 offset:18944
	ds_read_b128 v[198:201], v236 offset:20480
	ds_read_b128 v[186:189], v236 offset:20992
	ds_read_b128 v[182:185], v236 offset:22528
	ds_read_b128 v[178:181], v236 offset:23040
	v_sub_f32_e32 v36, v36, v66
	v_sub_f32_e32 v53, v53, v66
	v_sub_f32_e32 v37, v37, v66
	v_sub_f32_e32 v54, v54, v66
	v_sub_f32_e32 v38, v38, v66
	v_sub_f32_e32 v55, v55, v66
	v_sub_f32_e32 v39, v39, v66
	v_sub_f32_e32 v56, v56, v66
	v_sub_f32_e32 v40, v40, v66
	v_sub_f32_e32 v57, v57, v66
	v_sub_f32_e32 v41, v41, v66
	v_sub_f32_e32 v58, v58, v66
	v_sub_f32_e32 v42, v42, v66
	v_sub_f32_e32 v59, v59, v66
	v_sub_f32_e32 v43, v43, v66
	v_sub_f32_e32 v60, v60, v66
	v_sub_f32_e32 v44, v44, v66
	v_sub_f32_e32 v61, v61, v66
	v_sub_f32_e32 v45, v45, v66
	v_sub_f32_e32 v62, v62, v66
	v_sub_f32_e32 v46, v46, v66
	v_sub_f32_e32 v63, v63, v66
	v_sub_f32_e32 v47, v47, v66
	v_sub_f32_e32 v64, v64, v66
	v_sub_f32_e32 v48, v48, v66
	v_sub_f32_e32 v65, v65, v66
	v_sub_f32_e32 v49, v49, v66
	v_exp_f32_e32 v130, v50
	v_exp_f32_e32 v131, v51
	v_exp_f32_e32 v132, v52
	v_exp_f32_e32 v133, v53
	v_exp_f32_e32 v134, v54
	v_exp_f32_e32 v135, v55
	v_exp_f32_e32 v136, v56
	v_exp_f32_e32 v137, v57
	v_exp_f32_e32 v138, v58
	v_exp_f32_e32 v139, v59
	v_exp_f32_e32 v140, v60
	v_exp_f32_e32 v141, v61
	v_exp_f32_e32 v142, v62
	v_exp_f32_e32 v143, v63
	v_exp_f32_e32 v144, v64
	v_exp_f32_e32 v145, v65
	v_exp_f32_e32 v114, v34
	v_exp_f32_e32 v115, v35
	v_exp_f32_e32 v116, v36
	v_exp_f32_e32 v117, v37
	v_exp_f32_e32 v118, v38
	v_exp_f32_e32 v119, v39
	v_exp_f32_e32 v120, v40
	v_exp_f32_e32 v121, v41
	v_exp_f32_e32 v122, v42
	v_exp_f32_e32 v123, v43
	v_exp_f32_e32 v124, v44
	v_exp_f32_e32 v125, v45
	v_exp_f32_e32 v126, v46
	v_exp_f32_e32 v127, v47
	v_exp_f32_e32 v128, v48
	v_exp_f32_e32 v129, v49
	s_waitcnt vmcnt(4) lgkmcnt(0)
	s_barrier
	v_mov_b64_e32 v[80:81], v[16:17]
	v_mov_b64_e32 v[48:49], v[16:17]
	v_mov_b64_e32 v[64:65], v[16:17]
	v_mov_b64_e32 v[78:79], v[14:15]
	v_mov_b64_e32 v[76:77], v[12:13]
	v_mov_b64_e32 v[74:75], v[10:11]
	v_mov_b64_e32 v[72:73], v[8:9]
	v_mov_b64_e32 v[70:71], v[6:7]
	v_mov_b64_e32 v[68:69], v[4:5]
	v_mov_b64_e32 v[66:67], v[2:3]
	v_mov_b64_e32 v[46:47], v[14:15]
	v_mov_b64_e32 v[44:45], v[12:13]
	v_mov_b64_e32 v[42:43], v[10:11]
	v_mov_b64_e32 v[40:41], v[8:9]
	v_mov_b64_e32 v[38:39], v[6:7]
	v_mov_b64_e32 v[36:37], v[4:5]
	v_mov_b64_e32 v[34:35], v[2:3]
	v_mov_b64_e32 v[62:63], v[14:15]
	v_mov_b64_e32 v[60:61], v[12:13]
	v_mov_b64_e32 v[58:59], v[10:11]
	v_mov_b64_e32 v[56:57], v[8:9]
	v_mov_b64_e32 v[54:55], v[6:7]
	v_mov_b64_e32 v[52:53], v[4:5]
	v_mov_b64_e32 v[50:51], v[2:3]
	v_mov_b32_e32 v244, 0x23ee8
	ds_read2_b64 v[250:253], v244 offset1:1
	ds_read_b64 v[254:255], v244 offset:16
	s_waitcnt lgkmcnt(0)
	v_readfirstlane_b32 s68, v250
	v_readfirstlane_b32 s69, v251
	v_readfirstlane_b32 s70, v252
	v_readfirstlane_b32 s71, v253
	v_readfirstlane_b32 s72, v254
	v_readfirstlane_b32 s73, v255
	ds_read_b64 v[250:251], v244 offset:40
	s_waitcnt lgkmcnt(0)
	v_readfirstlane_b32 s74, v250
	v_readfirstlane_b32 s75, v251
	s_add_u32 s76, s74, 0x16530000
	s_addc_u32 s77, s75, 0
	s_add_u32 s74, s74, 0xa530000
	s_addc_u32 s75, s75, 0
	v_lshrrev_b32_e32 v25, 3, v214
	v_and_b32_e32 v28, 7, v214
	v_lshlrev_b32_e32 v33, 4, v28
	v_lshl_add_u32 v24, v25, 12, v33
	v_lshl_add_u32 v246, v25, 13, v33
	v_lshlrev_b32_e32 v29, 8, v28
	v_lshl_add_u32 v29, v25, 1, v29
	s_lshl_b32 s2, s40, 11
	s_add_i32 s2, s2, 0x20800
	v_add_u32_e32 v29, s2, v29
	v_add_u32_e32 v29, 32, v29
	v_lshl_add_u32 v32, v214, 3, s2
	s_mul_i32 s66, s96, 6
	s_add_i32 s66, s66, s40
	s_cmpk_lt_u32 s36, 0x100
	s_movk_i32 s67, 112
	s_cselect_b32 s67, 112, s67
	s_cselect_b32 s2, 0, 0x5400
	s_add_i32 s66, s66, s2
	s_cmp_lt_u32 s40, 6
	s_cselect_b32 s67, s67, 0
	global_load_dword v249, v24, s[68:69]
	global_load_dword v249, v24, s[68:69]

; __device__ __forceinline__ void convert_moe_items(const Ctx& a, int layer, LAS unsigned char* lds, int it0, int it1, int widx, int nw, int wave, int lane) {
;     ...
;     auto decode = [&](int it) { CvtItem d; const int e = it / PER_E; int r = it % PER_E; const size_t eo = ((size_t)layer * NE + e) * (size_t)DM * FE;
;         if (r < I_G)          { d.src = wg + eo; d.dst = WGU; d.N = FE; d.K = DM; d.row_off = e * 2048; d.ilv = 1; }
;         else if (r < 2 * I_G) { r -= I_G; d.src = wu + eo; d.dst = WGU; d.N = FE; d.K = DM; d.row_off = e * 2048 + 128; d.ilv = 1; }
;         else                  { r -= 2 * I_G; d.src = wd + eo; d.dst = WD; d.N = DM; d.K = FE; d.row_off = e * 2048; d.ilv = 0; }
;         const int nblk = d.N / 32; d.k0 = 64 * (r / nblk); d.n0 = 32 * (r % nblk); return d; };
.LBB0_529:
	v_mfma_f32_32x32x16_bf16 v[66:81], v[194:197], v[134:137], v[66:81]
	v_exp_f32_e32 v162, v162
	v_exp_f32_e32 v163, v163
	ds_read_b64_tr_b16 v[122:123], v16 offset:50176
	ds_read_b64_tr_b16 v[124:125], v16 offset:50688
	s_add_u32 s58, s33, 0xfef80000
	s_addc_u32 s59, s53, -1
	s_add_u32 s2, s33, 0xfefe0000
	s_addc_u32 s3, s53, -1
	s_add_i32 s60, s57, s49
	s_mov_b32 s61, m0
	s_mov_b32 m0, s60
	s_nop 0
	global_load_lds_dwordx4 v237, s[2:3] offset:0
	s_mov_b32 m0, s61
	v_mfma_f32_32x32x16_bf16 v[82:97], v[194:197], v[130:133], v[82:97]
	v_exp_f32_e32 v164, v164
	v_exp_f32_e32 v165, v165
	ds_read_b64_tr_b16 v[126:127], v16 offset:54272
	ds_read_b64_tr_b16 v[128:129], v16 offset:54784
	s_waitcnt lgkmcnt(6)
	v_mfma_f32_32x32x16_bf16 v[34:49], v[194:197], v[118:121], v[34:49]
	v_exp_f32_e32 v166, v166
	v_exp_f32_e32 v167, v167
	ds_read_b64_tr_b16 v[130:131], v16 offset:58368
	ds_read_b64_tr_b16 v[132:133], v16 offset:58880
	s_add_u32 s2, s33, 0xfefe0080
	s_addc_u32 s3, s53, -1
	s_add_i32 s60, s57, s54
	s_mov_b32 s61, m0
	s_mov_b32 m0, s60
	s_nop 0
	global_load_lds_dwordx4 v237, s[2:3] offset:0
	s_mov_b32 m0, s61
	s_waitcnt lgkmcnt(6)
	v_mfma_f32_32x32x16_bf16 v[50:65], v[194:197], v[114:117], v[50:65]
	v_exp_f32_e32 v168, v168
	v_exp_f32_e32 v169, v169
	ds_read_b64_tr_b16 v[118:119], v16 offset:62464
	ds_read_b64_tr_b16 v[120:121], v16 offset:62976
	v_add_u32_e32 v17, s55, v236
	ds_read_b128 v[114:117], v17
	ds_read_b128 v[178:181], v17 offset:512
	s_waitcnt lgkmcnt(8)
	v_mfma_f32_32x32x16_bf16 v[66:81], v[12:15], v[122:125], v[66:81]
	v_exp_f32_e32 v170, v170
	v_exp_f32_e32 v171, v171
	ds_read_b64_tr_b16 v[134:135], v16 offset:51200
	ds_read_b64_tr_b16 v[136:137], v16 offset:51712
	s_add_u32 s2, s33, 0x20000
	s_addc_u32 s3, s53, 0
	s_add_i32 s60, s55, s46
	s_mov_b32 s61, m0
	s_mov_b32 m0, s60
	s_nop 0
	global_load_lds_dwordx4 v235, s[2:3] offset:0
	s_mov_b32 m0, s61
	s_waitcnt lgkmcnt(8)
	v_mfma_f32_32x32x16_bf16 v[82:97], v[12:15], v[126:129], v[82:97]
	v_exp_f32_e32 v172, v172
	v_exp_f32_e32 v173, v173
	ds_read_b64_tr_b16 v[122:123], v16 offset:55296
	ds_read_b64_tr_b16 v[124:125], v16 offset:55808
	ds_read_b128 v[198:201], v17 offset:2048
	ds_read_b128 v[186:189], v17 offset:2560
	s_waitcnt lgkmcnt(10)
	v_mfma_f32_32x32x16_bf16 v[34:49], v[12:15], v[130:133], v[34:49]
	v_exp_f32_e32 v174, v174
	v_exp_f32_e32 v175, v175
	ds_read_b64_tr_b16 v[126:127], v16 offset:59392
	ds_read_b64_tr_b16 v[128:129], v16 offset:59904
	s_add_u32 s2, s33, 0x20080
	s_addc_u32 s3, s53, 0
	s_add_i32 s60, s55, s45
	s_mov_b32 s61, m0
	s_mov_b32 m0, s60
	s_nop 0
	global_load_lds_dwordx4 v235, s[2:3] offset:0
	s_mov_b32 m0, s61
	s_waitcnt lgkmcnt(10)
	v_mfma_f32_32x32x16_bf16 v[50:65], v[12:15], v[118:121], v[50:65]
	v_exp_f32_e32 v176, v176
	v_exp_f32_e32 v177, v177
	ds_read_b64_tr_b16 v[130:131], v16 offset:63488
	ds_read_b64_tr_b16 v[132:133], v16 offset:64000
	ds_read_b128 v[206:209], v17 offset:4096
	ds_read_b128 v[190:193], v17 offset:4608
	s_waitcnt lgkmcnt(10)
	v_mfma_f32_32x32x16_bf16 v[66:81], v[8:11], v[134:137], v[66:81]
	v_exp_f32_e32 v146, v146
	v_exp_f32_e32 v147, v147
	ds_read_b64_tr_b16 v[118:119], v16 offset:52224
	ds_read_b64_tr_b16 v[120:121], v16 offset:52736
	s_waitcnt lgkmcnt(10)
	v_mfma_f32_32x32x16_bf16 v[82:97], v[8:11], v[122:125], v[82:97]
	v_exp_f32_e32 v148, v148
	v_exp_f32_e32 v149, v149
	ds_read_b64_tr_b16 v[134:135], v16 offset:56320
	ds_read_b64_tr_b16 v[136:137], v16 offset:56832
	ds_read_b128 v[202:205], v17 offset:6144
	ds_read_b128 v[182:185], v17 offset:6656
	s_waitcnt lgkmcnt(10)
	v_mfma_f32_32x32x16_bf16 v[34:49], v[8:11], v[126:129], v[34:49]
	v_exp_f32_e32 v150, v150
	v_exp_f32_e32 v151, v151
	ds_read_b64_tr_b16 v[122:123], v16 offset:60416
	ds_read_b64_tr_b16 v[124:125], v16 offset:60928
	s_waitcnt lgkmcnt(10)
	v_mfma_f32_32x32x16_bf16 v[50:65], v[8:11], v[130:133], v[50:65]
	v_exp_f32_e32 v152, v152
	v_exp_f32_e32 v153, v153
	ds_read_b64_tr_b16 v[126:127], v16 offset:64512
	ds_read_b64_tr_b16 v[128:129], v16 offset:65024
	s_waitcnt lgkmcnt(8)
	v_mfma_f32_32x32x16_bf16 v[66:81], v[4:7], v[118:121], v[66:81]
	v_exp_f32_e32 v154, v154
	v_exp_f32_e32 v155, v155
	s_waitcnt vmcnt(6)
	v_cvt_pk_bf16_f32 v245, v250, v251
	v_cvt_pk_bf16_f32 v244, v252, v253
	s_add_i32 s2, s56, 1
	s_add_i32 s60, s2, -7
	s_cmp_lt_i32 s60, 0
	s_cbranch_scc1 .Lcs_dumS_h0
	s_cmp_ge_i32 s60, s67
	s_cbranch_scc1 .Lcs_dumS_h0
	s_and_b32 s61, s60, 7
	s_cmp_lg_u32 s61, 0
	s_cbranch_scc1 .Lcs_Sgo_h0
	s_mov_b64 s[100:101], s[64:65]
	v_mov_b32_e32 v28, v33
	s_mov_b32 s63, s88
	s_mov_b32 s87, s89
.Lcs_Sgo_h0:
	s_bitcmp1_b32 s60, 1
	s_cbranch_scc1 .Lcs_Shi_h0
	global_store_dwordx2 v28, v[30:31], s[100:101] nt
	s_branch .Lcs_Sadv_h0
.Lcs_Shi_h0:
	global_store_dwordx2 v28, v[26:27], s[100:101] nt
.Lcs_Sadv_h0:
	s_add_u32 s100, s100, s63
	s_addc_u32 s101, s101, 0
	s_and_b32 s61, s60, 3
	s_cmp_lg_u32 s61, 3
	s_cbranch_scc1 .Lcs_noS_h0
	s_sub_u32 s100, s100, s87
	s_subb_u32 s101, s101, 0
	s_branch .Lcs_noS_h0
.Lcs_dumS_h0:
	global_load_dword v249, v24, s[68:69]
.Lcs_noS_h0:
	s_cmp_ge_i32 s2, s67
	s_cbranch_scc1 .Lcs_dumL_h0
	s_and_b32 s61, s2, 7
	s_cmp_lg_u32 s61, 0
	s_cbranch_scc1 .Lcs_Lgo_h0
	s_mul_i32 s78, s66, 0xaaab
	s_lshr_b32 s78, s78, 27
	s_mul_i32 s79, s78, 0xc00
	s_sub_i32 s79, s66, s79
	s_addk_i32 s66, 0x600
	s_add_i32 s80, s78, 16
	s_lshl_b32 s80, s80, 23
	s_lshl_b32 s81, s78, 11
	s_cmpk_gt_u32 s79, 0x7ff
	s_cbranch_scc1 .Lcs_down_h0
	s_mov_b64 s[98:99], s[68:69]
	s_cmpk_gt_u32 s79, 0x3ff
	s_cbranch_scc0 .Lcs_gate_h0
	s_mov_b64 s[98:99], s[70:71]
	s_addk_i32 s81, 0x80
	s_addk_i32 s79, 0xfc00
.Lcs_gate_h0:
	s_add_u32 s98, s98, s80
	s_addc_u32 s99, s99, 0
	s_lshr_b32 s82, s79, 5
	s_lshl_b32 s82, s82, 6
	s_and_b32 s83, s79, 31
	s_lshl_b32 s83, s83, 5
	s_lshl_b32 s84, s82, 12
	s_lshl_b32 s85, s83, 2
	s_add_i32 s84, s84, s85
	s_add_u32 s98, s98, s84
	s_addc_u32 s99, s99, 0
	s_mov_b32 s62, 0x8000
	s_mov_b32 s88, 0x8000
	s_mov_b32 s89, 0x1ffc0
	s_lshr_b32 s84, s83, 7
	s_lshl_b32 s84, s84, 8
	s_and_b32 s85, s83, 0x7f
	s_add_i32 s84, s84, s85
	s_add_i32 s84, s84, s81
	s_lshl_b32 s84, s84, 12
	s_lshl_b32 s85, s82, 1
	s_add_i32 s84, s84, s85
	s_add_u32 s64, s74, s84
	s_addc_u32 s65, s75, 0
	v_mov_b32_e32 v25, v24
	v_lshrrev_b32_e32 v33, 1, v246
	s_branch .Lcs_Lgo_h0
.Lcs_down_h0:
	s_addk_i32 s79, 0xf800
	s_add_u32 s98, s72, s80
	s_addc_u32 s99, s73, 0
	s_lshr_b32 s82, s79, 6
	s_lshl_b32 s82, s82, 6
	s_and_b32 s83, s79, 63
	s_lshl_b32 s83, s83, 5
	s_lshl_b32 s84, s82, 13
	s_lshl_b32 s85, s83, 2
	s_add_i32 s84, s84, s85
	s_add_u32 s98, s98, s84
	s_addc_u32 s99, s99, 0
	s_mov_b32 s62, 0x10000
	s_mov_b32 s88, 0x4000
	s_mov_b32 s89, 0xffc0
	s_add_i32 s84, s81, s83
	s_lshl_b32 s84, s84, 11
	s_lshl_b32 s85, s82, 1
	s_add_i32 s84, s84, s85
	s_add_u32 s64, s76, s84
	s_addc_u32 s65, s77, 0
	v_mov_b32_e32 v25, v246
	v_lshrrev_b32_e32 v33, 1, v24
.Lcs_Lgo_h0:
	global_load_dwordx4 v[250:253], v25, s[98:99] nt
	s_add_u32 s98, s98, s62
	s_addc_u32 s99, s99, 0
	s_branch .Lcs_noL_h0

; #define LAS __attribute__((address_space(3)))
; __device__ __forceinline__ unsigned pk2(float lo, float hi) { return f2bf(lo) | (f2bf(hi) << 16); }
; #define WAIT_BAR(N) asm volatile("s_waitcnt vmcnt(" #N ") lgkmcnt(0)\n\ts_barrier" ::: "memory")
; #define RESC() do { if (resc) { asm volatile("s_waitcnt lgkmcnt(0)" ::: "memory"); \
;       _Pragma("unroll") for (int d_ = 0; d_ < 4; ++d_) _Pragma("unroll") for (int r = 0; r < 16; ++r) o[d_][r] *= wsf[crow(r, hi)]; } } while (0)
; #define ROT() do { sl_prev = sl_cur; sl_cur = sl_next; sl_next = (sl_next == (NSLOT - 1) * SLOTB) ? 0 : sl_next + SLOTB; } while (0)
;     __device__ __forceinline__ const float* x() const { return (const float*)ld(0); }
;     __device__ __forceinline__ const float* c() const { return (const float*)ld(1); }
; template <int THRL> ...
;     ...
;   int t = 1;
;   for (; t + 5 < NT; t += 2) {
;     STEP(pB0, pB1, pA0, pA1, t, true, true, true);     WAIT_BAR(4); RESC(); ROT();
; template <bool NT = true> __device__ __forceinline__ void cvt_store(const CvtItem& d, const f32x4 (&v)[8], LAS float* scr, int lane) {
;     const int rr = lane >> 3, c4 = (lane & 7) * 4;
; #pragma unroll
;     for (int q = 0; q < 8; ++q) { LAS float* t = scr + (8 * q + rr) * 33 + c4; t[0] = v[q].x; t[1] = v[q].y; t[2] = v[q].z; t[3] = v[q].w; }
;     asm volatile("s_waitcnt lgkmcnt(0)" ::: "memory");
;     const int c = lane & 7;
; #pragma unroll
;     for (int j = 0; j < 4; ++j) { const int n = (lane >> 3) + 8 * j; const LAS float* s = scr + (8 * c) * 33 + n;
;         u32x4 o; o.x = pk2(s[0 * 33], s[1 * 33]); o.y = pk2(s[2 * 33], s[3 * 33]); o.z = pk2(s[4 * 33], s[5 * 33]); o.w = pk2(s[6 * 33], s[7 * 33]);
;         const int ng = d.n0 + n, drow = d.row_off + (d.ilv ? ((ng >> 7) * 256 + (ng & 127)) : ng);
;         if (NT) __builtin_nontemporal_store(o, (u32x4*)(d.dst + (size_t)drow * d.K + d.k0 + 8 * c)); else *(u32x4*)(d.dst + (size_t)drow * d.K + d.k0 + 8 * c) = o; }
;     asm volatile("s_waitcnt lgkmcnt(0)" ::: "memory");
.Lcs_noL_h0:
	s_waitcnt lgkmcnt(6)
	v_mfma_f32_32x32x16_bf16 v[82:97], v[4:7], v[134:137], v[82:97]
	v_exp_f32_e32 v156, v156
	v_exp_f32_e32 v157, v157
	s_waitcnt lgkmcnt(2)
	v_mfma_f32_32x32x16_bf16 v[34:49], v[4:7], v[122:125], v[34:49]
	v_exp_f32_e32 v158, v158
	v_exp_f32_e32 v159, v159
	s_waitcnt lgkmcnt(0)
	v_mfma_f32_32x32x16_bf16 v[50:65], v[4:7], v[126:129], v[50:65]
	v_exp_f32_e32 v160, v160
	v_exp_f32_e32 v161, v161
	s_waitcnt lgkmcnt(0)
	s_cmp_eq_u32 s67, 0
	s_cbranch_scc1 .Lcs_noW_h0
	s_add_i32 s2, s56, 1
	s_bitcmp1_b32 s2, 1
	s_cbranch_scc0 .Lcs_noR_h0
	ds_read_b64 v[254:255], v32
	ds_read_b64 v[30:31], v32 offset:512
	ds_read_b64 v[22:23], v32 offset:1024
	ds_read_b64 v[26:27], v32 offset:1536
.Lcs_noR_h0:
	ds_write_b16 v29, v245
	ds_write_b16_d16_hi v29, v245 offset:64
	ds_write_b16 v29, v244 offset:128
	ds_write_b16_d16_hi v29, v244 offset:192
	s_and_b32 s3, s2, 3
	s_cmp_eq_u32 s3, 1
	s_cselect_b32 s3, -48, 16
	v_add_u32_e32 v29, s3, v29
.Lcs_noW_h0:
	s_barrier
	s_andn2_b64 vcc, exec, s[0:1]
	s_cbranch_vccnz .LBB0_531
	s_waitcnt lgkmcnt(0)
	v_add_u32_e32 v4, s50, v225
	ds_read_b128 v[118:121], v4 offset:96
	ds_read_b128 v[122:125], v4 offset:64
	ds_read_b128 v[126:129], v4 offset:32
	ds_read_b128 v[130:133], v4
	s_waitcnt lgkmcnt(3)
	v_pk_mul_f32 v[78:79], v[78:79], v[118:119]
	s_waitcnt lgkmcnt(2)
	v_pk_mul_f32 v[74:75], v[74:75], v[122:123]
	s_waitcnt lgkmcnt(1)
	v_pk_mul_f32 v[70:71], v[70:71], v[126:127]
	v_pk_mul_f32 v[80:81], v[80:81], v[120:121]
	v_pk_mul_f32 v[76:77], v[76:77], v[124:125]
	v_pk_mul_f32 v[72:73], v[72:73], v[128:129]
	s_waitcnt lgkmcnt(0)
	v_pk_mul_f32 v[68:69], v[68:69], v[132:133]
	v_pk_mul_f32 v[66:67], v[66:67], v[130:131]
	v_pk_mul_f32 v[94:95], v[94:95], v[118:119]
	v_pk_mul_f32 v[90:91], v[90:91], v[122:123]
	v_pk_mul_f32 v[86:87], v[86:87], v[126:127]
	v_pk_mul_f32 v[96:97], v[96:97], v[120:121]
	v_pk_mul_f32 v[92:93], v[92:93], v[124:125]
	v_pk_mul_f32 v[88:89], v[88:89], v[128:129]
	v_pk_mul_f32 v[84:85], v[84:85], v[132:133]
	v_pk_mul_f32 v[82:83], v[82:83], v[130:131]
	v_pk_mul_f32 v[46:47], v[46:47], v[118:119]
	v_pk_mul_f32 v[42:43], v[42:43], v[122:123]
	v_pk_mul_f32 v[38:39], v[38:39], v[126:127]
	v_pk_mul_f32 v[48:49], v[48:49], v[120:121]
	v_pk_mul_f32 v[44:45], v[44:45], v[124:125]
	v_pk_mul_f32 v[40:41], v[40:41], v[128:129]
	v_pk_mul_f32 v[36:37], v[36:37], v[132:133]
	v_pk_mul_f32 v[34:35], v[34:35], v[130:131]
	v_pk_mul_f32 v[62:63], v[62:63], v[118:119]
	v_pk_mul_f32 v[58:59], v[58:59], v[122:123]
	v_pk_mul_f32 v[54:55], v[54:55], v[126:127]
	v_pk_mul_f32 v[64:65], v[64:65], v[120:121]
	v_pk_mul_f32 v[60:61], v[60:61], v[124:125]
	v_pk_mul_f32 v[56:57], v[56:57], v[128:129]
	v_pk_mul_f32 v[52:53], v[52:53], v[132:133]
	v_pk_mul_f32 v[50:51], v[50:51], v[130:131]

; #define WAIT_BAR(N) asm volatile("s_waitcnt vmcnt(" #N ") lgkmcnt(0)\n\ts_barrier" ::: "memory")
; #define RESC() do { if (resc) { asm volatile("s_waitcnt lgkmcnt(0)" ::: "memory"); \
;       _Pragma("unroll") for (int d_ = 0; d_ < 4; ++d_) _Pragma("unroll") for (int r = 0; r < 16; ++r) o[d_][r] *= wsf[crow(r, hi)]; } } while (0)
; #define ROT() do { sl_prev = sl_cur; sl_cur = sl_next; sl_next = (sl_next == (NSLOT - 1) * SLOTB) ? 0 : sl_next + SLOTB; } while (0)
; template <int THRL> ...
;     ...
;   int t = 1;
;   for (; t + 5 < NT; t += 2) {
;     STEP(pB0, pB1, pA0, pA1, t, true, true, true);     WAIT_BAR(4); RESC(); ROT();
;     STEP(pA0, pA1, pB0, pB1, t + 1, true, true, true); WAIT_BAR(4); RESC(); ROT();
; __device__ __forceinline__ void convert_moe_items(const Ctx& a, int layer, LAS unsigned char* lds, int it0, int it1, int widx, int nw, int wave, int lane) {
;     ...
;     auto decode = [&](int it) { CvtItem d; const int e = it / PER_E; int r = it % PER_E; const size_t eo = ((size_t)layer * NE + e) * (size_t)DM * FE;
;         if (r < I_G)          { d.src = wg + eo; d.dst = WGU; d.N = FE; d.K = DM; d.row_off = e * 2048; d.ilv = 1; }
;         else if (r < 2 * I_G) { r -= I_G; d.src = wu + eo; d.dst = WGU; d.N = FE; d.K = DM; d.row_off = e * 2048 + 128; d.ilv = 1; }
;         else                  { r -= 2 * I_G; d.src = wd + eo; d.dst = WD; d.N = DM; d.K = FE; d.row_off = e * 2048; d.ilv = 0; }
;         const int nblk = d.N / 32; d.k0 = 64 * (r / nblk); d.n0 = 32 * (r % nblk); return d; };
.LBB0_532:
	s_add_i32 s2, s55, 0x4000
	s_cmpk_lg_u32 s55, 0x8000
	s_cselect_b32 s57, s2, 0
	v_mfma_f32_32x32x16_bf16 v[66:81], v[194:197], v[166:169], v[66:81]
	v_exp_f32_e32 v130, v130
	v_exp_f32_e32 v131, v131
	ds_read_b64_tr_b16 v[154:155], v16 offset:50176
	ds_read_b64_tr_b16 v[156:157], v16 offset:50688
	s_add_u32 s2, s58, 0x80000
	s_addc_u32 s3, s59, 0
	s_add_i32 s60, s55, s49
	s_mov_b32 s61, m0
	s_mov_b32 m0, s60
	s_nop 0
	global_load_lds_dwordx4 v237, s[2:3] offset:0
	s_mov_b32 m0, s61
	v_mfma_f32_32x32x16_bf16 v[82:97], v[194:197], v[162:165], v[82:97]
	v_exp_f32_e32 v132, v132
	v_exp_f32_e32 v133, v133
	ds_read_b64_tr_b16 v[158:159], v16 offset:54272
	ds_read_b64_tr_b16 v[160:161], v16 offset:54784
	s_waitcnt lgkmcnt(6)
	v_mfma_f32_32x32x16_bf16 v[34:49], v[194:197], v[150:153], v[34:49]
	v_exp_f32_e32 v134, v134
	v_exp_f32_e32 v135, v135
	ds_read_b64_tr_b16 v[162:163], v16 offset:58368
	ds_read_b64_tr_b16 v[164:165], v16 offset:58880
	s_add_u32 s2, s58, 0x80080
	s_addc_u32 s3, s59, 0
	s_add_i32 s58, s55, s54
	s_mov_b32 s59, m0
	s_mov_b32 m0, s58
	s_nop 0
	global_load_lds_dwordx4 v237, s[2:3] offset:0
	s_mov_b32 m0, s59
	s_waitcnt lgkmcnt(6)
	v_mfma_f32_32x32x16_bf16 v[50:65], v[194:197], v[146:149], v[50:65]
	v_exp_f32_e32 v136, v136
	v_exp_f32_e32 v137, v137
	ds_read_b64_tr_b16 v[150:151], v16 offset:62464
	ds_read_b64_tr_b16 v[152:153], v16 offset:62976
	v_add_u32_e32 v3, s57, v236
	ds_read_b128 v[146:149], v3
	ds_read_b128 v[202:205], v3 offset:512
	s_waitcnt lgkmcnt(8)
	v_mfma_f32_32x32x16_bf16 v[66:81], v[12:15], v[154:157], v[66:81]
	v_exp_f32_e32 v138, v138
	v_exp_f32_e32 v139, v139
	ds_read_b64_tr_b16 v[166:167], v16 offset:51200
	ds_read_b64_tr_b16 v[168:169], v16 offset:51712
	s_add_u32 s2, s33, 0x40000
	s_addc_u32 s3, s53, 0
	s_add_i32 s58, s57, s46
	s_mov_b32 s59, m0
	s_mov_b32 m0, s58
	s_nop 0
	global_load_lds_dwordx4 v235, s[2:3] offset:0
	s_mov_b32 m0, s59
	s_waitcnt lgkmcnt(8)
	v_mfma_f32_32x32x16_bf16 v[82:97], v[12:15], v[158:161], v[82:97]
	v_exp_f32_e32 v140, v140
	v_exp_f32_e32 v141, v141
	ds_read_b64_tr_b16 v[154:155], v16 offset:55296
	ds_read_b64_tr_b16 v[156:157], v16 offset:55808
	ds_read_b128 v[206:209], v3 offset:2048
	ds_read_b128 v[190:193], v3 offset:2560
	s_waitcnt lgkmcnt(10)
	v_mfma_f32_32x32x16_bf16 v[34:49], v[12:15], v[162:165], v[34:49]
	v_exp_f32_e32 v142, v142
	v_exp_f32_e32 v143, v143
	ds_read_b64_tr_b16 v[158:159], v16 offset:59392
	ds_read_b64_tr_b16 v[160:161], v16 offset:59904
	s_add_u32 s2, s33, 0x40080
	s_addc_u32 s3, s53, 0
	s_add_i32 s58, s57, s45
	s_mov_b32 s59, m0
	s_mov_b32 m0, s58
	s_nop 0
	global_load_lds_dwordx4 v235, s[2:3] offset:0
	s_mov_b32 m0, s59
	s_waitcnt lgkmcnt(10)
	v_mfma_f32_32x32x16_bf16 v[50:65], v[12:15], v[150:153], v[50:65]
	v_exp_f32_e32 v144, v144
	v_exp_f32_e32 v145, v145
	ds_read_b64_tr_b16 v[162:163], v16 offset:63488
	ds_read_b64_tr_b16 v[164:165], v16 offset:64000
	ds_read_b128 v[198:201], v3 offset:4096
	ds_read_b128 v[186:189], v3 offset:4608
	s_waitcnt lgkmcnt(10)
	v_mfma_f32_32x32x16_bf16 v[66:81], v[8:11], v[166:169], v[66:81]
	v_exp_f32_e32 v114, v114
	v_exp_f32_e32 v115, v115
	ds_read_b64_tr_b16 v[150:151], v16 offset:52224
	ds_read_b64_tr_b16 v[152:153], v16 offset:52736
	s_waitcnt lgkmcnt(10)
	v_mfma_f32_32x32x16_bf16 v[82:97], v[8:11], v[154:157], v[82:97]
	v_exp_f32_e32 v116, v116
	v_exp_f32_e32 v117, v117
	ds_read_b64_tr_b16 v[166:167], v16 offset:56320
	ds_read_b64_tr_b16 v[168:169], v16 offset:56832
	ds_read_b128 v[182:185], v3 offset:6144
	ds_read_b128 v[178:181], v3 offset:6656
	s_waitcnt lgkmcnt(10)
	v_mfma_f32_32x32x16_bf16 v[34:49], v[8:11], v[158:161], v[34:49]
	v_exp_f32_e32 v118, v118
	v_exp_f32_e32 v119, v119
	ds_read_b64_tr_b16 v[154:155], v16 offset:60416
	ds_read_b64_tr_b16 v[156:157], v16 offset:60928
	s_waitcnt lgkmcnt(10)
	v_mfma_f32_32x32x16_bf16 v[50:65], v[8:11], v[162:165], v[50:65]
	v_exp_f32_e32 v120, v120
	v_exp_f32_e32 v121, v121
	ds_read_b64_tr_b16 v[158:159], v16 offset:64512
	ds_read_b64_tr_b16 v[160:161], v16 offset:65024
	s_waitcnt lgkmcnt(8)
	v_mfma_f32_32x32x16_bf16 v[66:81], v[4:7], v[150:153], v[66:81]
	v_exp_f32_e32 v122, v122
	v_exp_f32_e32 v123, v123
	s_waitcnt vmcnt(6)
	v_cvt_pk_bf16_f32 v245, v18, v19
	v_cvt_pk_bf16_f32 v244, v20, v21
	s_add_i32 s2, s56, 2
	s_add_i32 s60, s2, -7
	s_cmp_lt_i32 s60, 0
	s_cbranch_scc1 .Lcs_dumS_h1
	s_cmp_ge_i32 s60, s67
	s_cbranch_scc1 .Lcs_dumS_h1
	s_and_b32 s61, s60, 7
	s_cmp_lg_u32 s61, 0
	s_cbranch_scc1 .Lcs_Sgo_h1
	s_mov_b64 s[100:101], s[64:65]
	v_mov_b32_e32 v28, v33
	s_mov_b32 s63, s88
	s_mov_b32 s87, s89
.Lcs_Sgo_h1:
	s_bitcmp1_b32 s60, 1
	s_cbranch_scc1 .Lcs_Shi_h1
	global_store_dwordx2 v28, v[254:255], s[100:101] nt
	s_branch .Lcs_Sadv_h1
.Lcs_Shi_h1:
	global_store_dwordx2 v28, v[22:23], s[100:101] nt

; __device__ __forceinline__ void cvt_load(const CvtItem& d, f32x4 (&v)[8], int lane) {
;     const float* p = d.src + (size_t)(d.k0 + (lane >> 3)) * d.N + d.n0 + (lane & 7) * 4;
; #pragma unroll
;     for (int q = 0; q < 8; ++q) v[q] = __builtin_nontemporal_load((const f32x4*)(p + (size_t)(8 * q) * d.N));
; }
.Lcs_Lgo_h1:
	global_load_dwordx4 v[18:21], v25, s[98:99] nt
	s_add_u32 s98, s98, s62
	s_addc_u32 s99, s99, 0
	s_branch .Lcs_noL_h1

; #define LAS __attribute__((address_space(3)))
; __device__ __forceinline__ unsigned pk2(float lo, float hi) { return f2bf(lo) | (f2bf(hi) << 16); }
; #define WAIT_BAR(N) asm volatile("s_waitcnt vmcnt(" #N ") lgkmcnt(0)\n\ts_barrier" ::: "memory")
; #define RESC() do { if (resc) { asm volatile("s_waitcnt lgkmcnt(0)" ::: "memory"); \
;       _Pragma("unroll") for (int d_ = 0; d_ < 4; ++d_) _Pragma("unroll") for (int r = 0; r < 16; ++r) o[d_][r] *= wsf[crow(r, hi)]; } } while (0)
; #define ROT() do { sl_prev = sl_cur; sl_cur = sl_next; sl_next = (sl_next == (NSLOT - 1) * SLOTB) ? 0 : sl_next + SLOTB; } while (0)
;     __device__ __forceinline__ const float* x() const { return (const float*)ld(0); }
;     __device__ __forceinline__ const float* c() const { return (const float*)ld(1); }
; template <int THRL> ...
;     ...
;   int t = 1;
;   for (; t + 5 < NT; t += 2) {
;     STEP(pB0, pB1, pA0, pA1, t, true, true, true);     WAIT_BAR(4); RESC(); ROT();
;     STEP(pA0, pA1, pB0, pB1, t + 1, true, true, true); WAIT_BAR(4); RESC(); ROT();
; template <bool NT = true> __device__ __forceinline__ void cvt_store(const CvtItem& d, const f32x4 (&v)[8], LAS float* scr, int lane) {
;     const int rr = lane >> 3, c4 = (lane & 7) * 4;
; #pragma unroll
;     for (int q = 0; q < 8; ++q) { LAS float* t = scr + (8 * q + rr) * 33 + c4; t[0] = v[q].x; t[1] = v[q].y; t[2] = v[q].z; t[3] = v[q].w; }
;     asm volatile("s_waitcnt lgkmcnt(0)" ::: "memory");
;     const int c = lane & 7;
; #pragma unroll
;     for (int j = 0; j < 4; ++j) { const int n = (lane >> 3) + 8 * j; const LAS float* s = scr + (8 * c) * 33 + n;
;         u32x4 o; o.x = pk2(s[0 * 33], s[1 * 33]); o.y = pk2(s[2 * 33], s[3 * 33]); o.z = pk2(s[4 * 33], s[5 * 33]); o.w = pk2(s[6 * 33], s[7 * 33]);
;         const int ng = d.n0 + n, drow = d.row_off + (d.ilv ? ((ng >> 7) * 256 + (ng & 127)) : ng);
;         if (NT) __builtin_nontemporal_store(o, (u32x4*)(d.dst + (size_t)drow * d.K + d.k0 + 8 * c)); else *(u32x4*)(d.dst + (size_t)drow * d.K + d.k0 + 8 * c) = o; }
;     asm volatile("s_waitcnt lgkmcnt(0)" ::: "memory");
.Lcs_noL_h1:
	s_waitcnt lgkmcnt(6)
	v_mfma_f32_32x32x16_bf16 v[82:97], v[4:7], v[166:169], v[82:97]
	v_exp_f32_e32 v124, v124
	v_exp_f32_e32 v125, v125
	s_waitcnt lgkmcnt(2)
	v_mfma_f32_32x32x16_bf16 v[34:49], v[4:7], v[154:157], v[34:49]
	v_exp_f32_e32 v126, v126
	v_exp_f32_e32 v127, v127
	s_waitcnt lgkmcnt(0)
	v_mfma_f32_32x32x16_bf16 v[50:65], v[4:7], v[158:161], v[50:65]
	v_exp_f32_e32 v128, v128
	v_exp_f32_e32 v129, v129
	s_waitcnt lgkmcnt(0)
	s_cmp_eq_u32 s67, 0
	s_cbranch_scc1 .Lcs_noW_h1
	s_add_i32 s2, s56, 2
	ds_write_b16 v29, v245
	ds_write_b16_d16_hi v29, v245 offset:64
	ds_write_b16 v29, v244 offset:128
	ds_write_b16_d16_hi v29, v244 offset:192
	s_and_b32 s3, s2, 3
	s_cmp_eq_u32 s3, 1
	s_cselect_b32 s3, -48, 16
	v_add_u32_e32 v29, s3, v29
.Lcs_noW_h1:
	s_barrier
	s_andn2_b64 vcc, exec, s[0:1]
	s_cbranch_vccnz .LBB0_534
	s_waitcnt lgkmcnt(0)
	v_add_u32_e32 v3, s50, v225
	ds_read_b128 v[150:153], v3 offset:96
	ds_read_b128 v[154:157], v3 offset:64
	ds_read_b128 v[158:161], v3 offset:32
	ds_read_b128 v[162:165], v3
	s_waitcnt lgkmcnt(3)
	v_pk_mul_f32 v[78:79], v[78:79], v[150:151]
	s_waitcnt lgkmcnt(2)
	v_pk_mul_f32 v[74:75], v[74:75], v[154:155]
	s_waitcnt lgkmcnt(1)
	v_pk_mul_f32 v[70:71], v[70:71], v[158:159]
	v_pk_mul_f32 v[80:81], v[80:81], v[152:153]
	v_pk_mul_f32 v[76:77], v[76:77], v[156:157]
	v_pk_mul_f32 v[72:73], v[72:73], v[160:161]
	s_waitcnt lgkmcnt(0)
	v_pk_mul_f32 v[68:69], v[68:69], v[164:165]
	v_pk_mul_f32 v[66:67], v[66:67], v[162:163]
	v_pk_mul_f32 v[94:95], v[94:95], v[150:151]
	v_pk_mul_f32 v[90:91], v[90:91], v[154:155]
	v_pk_mul_f32 v[86:87], v[86:87], v[158:159]
	v_pk_mul_f32 v[96:97], v[96:97], v[152:153]
	v_pk_mul_f32 v[92:93], v[92:93], v[156:157]
	v_pk_mul_f32 v[88:89], v[88:89], v[160:161]
	v_pk_mul_f32 v[84:85], v[84:85], v[164:165]
	v_pk_mul_f32 v[82:83], v[82:83], v[162:163]
	v_pk_mul_f32 v[46:47], v[46:47], v[150:151]
	v_pk_mul_f32 v[42:43], v[42:43], v[154:155]
	v_pk_mul_f32 v[38:39], v[38:39], v[158:159]
	v_pk_mul_f32 v[48:49], v[48:49], v[152:153]
	v_pk_mul_f32 v[44:45], v[44:45], v[156:157]
	v_pk_mul_f32 v[40:41], v[40:41], v[160:161]
	v_pk_mul_f32 v[36:37], v[36:37], v[164:165]
	v_pk_mul_f32 v[34:35], v[34:35], v[162:163]
	v_pk_mul_f32 v[62:63], v[62:63], v[150:151]
	v_pk_mul_f32 v[58:59], v[58:59], v[154:155]
	v_pk_mul_f32 v[54:55], v[54:55], v[158:159]
	v_pk_mul_f32 v[64:65], v[64:65], v[152:153]
	v_pk_mul_f32 v[60:61], v[60:61], v[156:157]
	v_pk_mul_f32 v[56:57], v[56:57], v[160:161]
	v_pk_mul_f32 v[52:53], v[52:53], v[164:165]
	v_pk_mul_f32 v[50:51], v[50:51], v[162:163]

.LBB0_542:
	v_mov_b32_e32 v18, 0
	v_mov_b32_e32 v19, 0
	v_mov_b32_e32 v20, 0
	v_mov_b32_e32 v21, 0
	v_mov_b32_e32 v22, 0
	v_mov_b32_e32 v23, 0
	v_mov_b32_e32 v24, 0
	v_mov_b32_e32 v25, 0
	v_mov_b32_e32 v26, 0
	v_mov_b32_e32 v27, 0
	v_mov_b32_e32 v28, 0
	v_mov_b32_e32 v29, 0
	v_mov_b32_e32 v30, 0
	v_mov_b32_e32 v31, 0
	v_mov_b32_e32 v32, 0
	v_mov_b32_e32 v33, 0
	ds_read_b128 v[240:243], v233
	v_add_f32_e32 v3, v130, v131
	v_add_f32_e32 v3, v132, v3
	v_add_f32_e32 v3, v133, v3
	v_add_f32_e32 v3, v134, v3
	s_waitcnt lgkmcnt(0)
	v_mfma_f32_32x32x16_bf16 v[162:177], v[146:149], v[240:243], v[98:113]
	v_add_f32_e32 v3, v135, v3
	v_cvt_pk_bf16_f32 v194, v130, v131
	v_cvt_pk_bf16_f32 v195, v132, v133
	v_mfma_f32_32x32x16_bf16 v[146:161], v[202:205], v[240:243], v[98:113]
	v_add_f32_e32 v3, v136, v3
	v_add_f32_e32 v3, v137, v3
	v_add_f32_e32 v3, v138, v3
	v_add_f32_e32 v3, v139, v3
	v_cvt_pk_bf16_f32 v196, v134, v135
	v_cvt_pk_bf16_f32 v197, v136, v137
	ds_read_b128 v[130:133], v233 offset:1024
	v_add_f32_e32 v3, v140, v3
	v_add_f32_e32 v3, v141, v3
	v_add_f32_e32 v3, v142, v3
	v_add_f32_e32 v3, v143, v3
	s_waitcnt lgkmcnt(0)
	v_mfma_f32_32x32x16_bf16 v[162:177], v[206:209], v[130:133], v[162:177]
	v_cvt_pk_bf16_f32 v12, v138, v139
	v_cvt_pk_bf16_f32 v13, v140, v141
	v_mfma_f32_32x32x16_bf16 v[146:161], v[190:193], v[130:133], v[146:161]
	v_add_f32_e32 v3, v144, v3
	v_add_f32_e32 v3, v145, v3
	v_add_f32_e32 v3, v114, v3
	v_add_f32_e32 v3, v115, v3
	v_cvt_pk_bf16_f32 v14, v142, v143
	v_cvt_pk_bf16_f32 v15, v144, v145
	ds_read_b128 v[138:141], v233 offset:2048
	ds_read_b64_tr_b16 v[134:135], v223 offset:49152
	ds_read_b64_tr_b16 v[136:137], v223 offset:49664
	s_waitcnt lgkmcnt(2)
	v_mfma_f32_32x32x16_bf16 v[162:177], v[198:201], v[138:141], v[162:177]
	v_add_f32_e32 v3, v116, v3
	v_add_f32_e32 v3, v117, v3
	v_add_f32_e32 v3, v118, v3
	v_add_f32_e32 v3, v119, v3
	v_cvt_pk_bf16_f32 v8, v114, v115
	v_cvt_pk_bf16_f32 v9, v116, v117
	ds_read_b64_tr_b16 v[130:131], v223 offset:53248
	ds_read_b64_tr_b16 v[132:133], v223 offset:53760
	v_mfma_f32_32x32x16_bf16 v[146:161], v[186:189], v[138:141], v[146:161]
	v_add_f32_e32 v3, v120, v3
	v_add_f32_e32 v3, v121, v3
	v_add_f32_e32 v3, v122, v3
	v_add_f32_e32 v3, v123, v3
	v_cvt_pk_bf16_f32 v10, v118, v119
	v_cvt_pk_bf16_f32 v11, v120, v121
	ds_read_b128 v[138:141], v233 offset:3072
	ds_read_b64_tr_b16 v[118:119], v223 offset:57344
	ds_read_b64_tr_b16 v[120:121], v223 offset:57856
	s_waitcnt lgkmcnt(2)
	v_mfma_f32_32x32x16_bf16 v[162:177], v[182:185], v[138:141], v[162:177]
	v_add_f32_e32 v3, v124, v3
	v_add_f32_e32 v3, v125, v3
	v_add_f32_e32 v3, v126, v3
	v_add_f32_e32 v3, v127, v3
	v_cvt_pk_bf16_f32 v4, v122, v123
	v_cvt_pk_bf16_f32 v5, v124, v125
	ds_read_b64_tr_b16 v[114:115], v223 offset:61440
	ds_read_b64_tr_b16 v[116:117], v223 offset:61952
	v_mfma_f32_32x32x16_bf16 v[146:161], v[178:181], v[138:141], v[146:161]
	v_add_f32_e32 v3, v128, v3
	v_add_f32_e32 v3, v129, v3
	v_add_f32_e32 v3, 0, v3
	v_cvt_pk_bf16_f32 v6, v126, v127
	v_cvt_pk_bf16_f32 v7, v128, v129
	v_max_f32_e32 v16, v163, v163
	v_max_f32_e32 v17, v162, v162
	v_max_f32_e32 v16, v17, v16
	s_nop 3
	v_max3_f32 v17, v164, v165, v147
	v_max3_f32 v16, v16, v146, v148
	v_max3_f32 v16, v16, v149, v166
	v_max3_f32 v17, v17, v168, v169
	v_max3_f32 v16, v16, v167, v150
	v_max3_f32 v17, v17, v152, v153
	v_max3_f32 v16, v16, v151, v170
	v_max3_f32 v17, v17, v172, v173
	v_max3_f32 v16, v16, v171, v154
	v_max3_f32 v17, v17, v156, v157
	v_max3_f32 v16, v16, v155, v174
	v_max3_f32 v17, v17, v176, v177
	v_max3_f32 v122, v16, v175, v158
	v_max3_f32 v17, v17, v160, v161
	v_add_f32_e32 v16, v238, v3
	v_max3_f32 v3, v122, v159, v17
	v_mov_b32_e32 v17, v3
	s_nop 1
	v_permlane32_swap_b32_e32 v3, v17
	v_max_f32_e32 v17, v17, v17
	v_max_f32_e32 v3, v3, v3
	v_max_f32_e32 v3, v3, v17
	v_cmp_lt_f32_e32 vcc, s30, v3
	s_cmp_lg_u64 vcc, 0
	s_cselect_b64 s[0:1], -1, 0
	s_cbranch_vccnz .LBB0_565

;     __device__ __forceinline__ const float* x() const { return (const float*)ld(0); }
;     __device__ __forceinline__ unsigned char* ws() const { return (unsigned char*)ld(26); }
; PHASE_FN ph_wout(unsigned* dep, const XcdBarrier& bar) { PH_PRO;
;     unsigned char* ws = a.ws();
;     const int GH = (G >= 2) ? G / 2 : G;
;     if ((int)blockIdx.x < GH) {
;         if (dep) dep_wait(dep, bar);
;         const pg8::Geo g = pg8::geo_rowmajor(ws + WS_CAT, DM, ws + WS_WOUT, DM, DM);
;         pg8::StaticOrder S; S.init(SEQ, DM, GH, (int)blockIdx.x);
;         pg8::EpiResid<true> E{a.x(), (_Float16*)(ws + WS_X), (const float*)(ws + WS_MODL) + 2 * DM};
;         pg8::gemm_phase<pg8::EpiResid<true>, pg8::StaticOrder, true, true>(lds, g, S, E);
;         if (GH == G) convert_moe_items(a, 1, lds, 0, L1_A, gw, NGW, wave, lane);
;     } else convert_moe_items(a, 1, lds, 0, L1_A, ((int)blockIdx.x - GH) * NWAVES + wave, (G - GH) * NWAVES, wave, lane);
.LBB0_650:
	s_cmp_lt_i32 s94, 5
	s_cselect_b64 s[2:3], -1, 0
	s_and_b64 s[8:9], s[2:3], s[0:1]
	s_andn2_b64 vcc, exec, s[8:9]
	s_cbranch_vccnz .LBB0_791
	v_readlane_b32 s0, v248, 0
	v_readlane_b32 s1, v248, 1
	s_load_dword s43, s[0:1], 0xe0
	s_add_i32 s0, 0, 0x23f10
	v_mov_b32_e32 v1, s0
	v_readfirstlane_b32 s0, v0
	s_lshr_b32 s44, s0, 6
	s_waitcnt lgkmcnt(0)
	s_lshl_b32 s42, s43, 3
	s_waitcnt vmcnt(0)
	ds_read_b64 v[2:3], v1
	s_cmp_gt_i32 s43, 1
	s_cselect_b64 s[0:1], -1, 0
	v_cndmask_b32_e64 v1, 0, 1, s[0:1]
	s_waitcnt lgkmcnt(0)
	v_readfirstlane_b32 s30, v3
	v_readfirstlane_b32 s0, v1
	s_mov_b32 s45, s43
	v_readfirstlane_b32 s31, v2
	s_cmp_ge_i32 s96, s45
	s_mov_b64 s[0:1], -1
	s_cbranch_scc0 .LBB0_699
	s_sub_i32 s0, s96, s45
	s_lshl_b32 s0, s0, 3
	s_add_i32 s41, s0, s44
	s_add_i32 s0, 0, 0x23ee8
	v_mov_b32_e32 v1, s0
	s_add_i32 s0, 0, 0x23ef8
	ds_read2_b64 v[4:7], v1 offset1:1
	v_mov_b32_e32 v1, s0
	v_readfirstlane_b32 s2, v3
	v_readfirstlane_b32 s3, v2
	ds_read_b64 v[2:3], v1
	s_waitcnt lgkmcnt(1)
	v_readfirstlane_b32 s33, v5
	v_readfirstlane_b32 s34, v4
	v_readfirstlane_b32 s35, v7
	v_readfirstlane_b32 s36, v6
	s_waitcnt lgkmcnt(0)
	v_readfirstlane_b32 s37, v3
	s_cmpk_gt_u32 s41, 0xa7ff
	v_readfirstlane_b32 s38, v2
	s_cbranch_scc1 .LBB0_698
	s_add_u32 s0, s3, 0xa530000
	s_addc_u32 s1, s2, 0
	s_add_u32 s4, s3, 0x16530000
	s_addc_u32 s5, s2, 0
	s_and_b32 s2, s41, 0xffff
	s_mul_i32 s2, s2, 0xaaab
	s_lshr_b32 s2, s2, 27
	s_mul_i32 s3, s2, 0xc00
	s_sub_i32 s3, s41, s3
	s_lshl_b32 s18, s2, 21
	s_and_b32 s14, s3, 0xffff
	s_add_i32 s18, s18, 0x2000000
	s_lshl_b32 s15, s2, 11
	s_cmpk_gt_u32 s14, 0x3ff
	s_cbranch_scc0 .LBB0_657
	s_cmpk_gt_u32 s14, 0x7ff
	s_cbranch_scc0 .LBB0_663
	s_add_i32 s17, s14, 0xfffff800
	s_lshl_b32 s2, s18, 2
	s_add_u32 s2, s38, s2
	s_addc_u32 s3, s37, 0
	s_mov_b32 s29, 1
	s_cbranch_execz .LBB0_664
	s_movk_i32 s16, 0x800
	s_movk_i32 s39, 0x400
	s_mov_b32 s29, 0
	s_mov_b32 s40, s15
	s_mov_b64 s[10:11], s[4:5]
	s_cbranch_execz .LBB0_658
	s_branch .LBB0_659

;     __device__ __forceinline__ const float* x() const { return (const float*)ld(0); }
; PHASE_FN ph_wout(unsigned* dep, const XcdBarrier& bar) { PH_PRO;
;     ...
;         pg8::gemm_phase<pg8::EpiResid<true>, pg8::StaticOrder, true, true>(lds, g, S, E);
;         if (GH == G) convert_moe_items(a, 1, lds, 0, L1_A, gw, NGW, wave, lane);
;     } else convert_moe_items(a, 1, lds, 0, L1_A, ((int)blockIdx.x - GH) * NWAVES + wave, (G - GH) * NWAVES, wave, lane);
.LBB0_741:
	s_cmp_lg_u32 s43, s45
	s_branch .LBB0_791
	s_add_i32 s1, 0, 0x23f10
	v_mov_b32_e32 v2, s1
	s_waitcnt vmcnt(6)
	ds_read_b64 v[6:7], v2
	s_lshl_b32 s0, s96, 3
	s_add_i32 s37, s44, s0
	s_add_i32 s0, 0, 0x23ee8
	v_mov_b32_e32 v2, s0
	s_add_i32 s0, 0, 0x23ef8
	s_waitcnt lgkmcnt(0)
	v_readfirstlane_b32 s3, v6
	v_mov_b32_e32 v6, s0
	ds_read2_b64 v[2:5], v2 offset1:1
	v_readfirstlane_b32 s2, v7
	ds_read_b64 v[6:7], v6
	s_cmp_gt_i32 s37, 0xa7ff
	s_waitcnt lgkmcnt(1)
	v_readfirstlane_b32 s28, v3
	v_readfirstlane_b32 s29, v2
	v_readfirstlane_b32 s30, v5
	v_readfirstlane_b32 s31, v4
	s_waitcnt lgkmcnt(0)
	v_readfirstlane_b32 s33, v7
	v_readfirstlane_b32 s34, v6
	s_cbranch_scc1 .LBB0_791
	s_add_u32 s0, s3, 0xa530000
	s_addc_u32 s1, s2, 0
	s_add_u32 s4, s3, 0x16530000
	s_addc_u32 s5, s2, 0
	s_mul_hi_i32 s2, s37, 0x2aaaaaab
	s_lshr_b32 s3, s2, 31
	s_ashr_i32 s2, s2, 9
	s_add_i32 s2, s2, s3
	s_mul_i32 s3, s2, 0xc00
	s_sub_i32 s15, s37, s3
	s_ashr_i32 s3, s2, 31
	s_lshl_b64 s[6:7], s[2:3], 21
	s_add_u32 s10, s6, 0x2000000
	s_addc_u32 s11, s7, 0
	s_lshl_b32 s17, s2, 11
	s_cmpk_gt_i32 s15, 0x3ff
	s_cbranch_scc0 .LBB0_746
	s_cmpk_gt_u32 s15, 0x7ff
	s_cbranch_scc0 .LBB0_747
	s_add_i32 s16, s15, 0xfffff800
	s_lshl_b64 s[2:3], s[10:11], 2
	s_add_u32 s2, s34, s2
	s_addc_u32 s3, s33, s3
	s_mov_b64 s[6:7], 0
	s_branch .LBB0_748

; __global__ void __launch_bounds__(NTHR, 2) fwd(Args ka) {
	.amdhsa_kernel _Z3fwd4Args
		.amdhsa_group_segment_fixed_size 0
		.amdhsa_private_segment_fixed_size 0
		.amdhsa_kernarg_size 480
		.amdhsa_user_sgpr_count 2
		.amdhsa_user_sgpr_dispatch_ptr 0
		.amdhsa_user_sgpr_queue_ptr 0
		.amdhsa_user_sgpr_kernarg_segment_ptr 1
		.amdhsa_user_sgpr_dispatch_id 0
		.amdhsa_user_sgpr_kernarg_preload_length 0
		.amdhsa_user_sgpr_kernarg_preload_offset 0
		.amdhsa_user_sgpr_private_segment_size 0
		.amdhsa_uses_dynamic_stack 0
		.amdhsa_enable_private_segment 0
		.amdhsa_system_sgpr_workgroup_id_x 1
		.amdhsa_system_sgpr_workgroup_id_y 0
		.amdhsa_system_sgpr_workgroup_id_z 0
		.amdhsa_system_sgpr_workgroup_info 0
		.amdhsa_system_vgpr_workitem_id 0
		.amdhsa_next_free_vgpr 256
		.amdhsa_next_free_sgpr 102
		.amdhsa_accum_offset 256
		.amdhsa_reserve_vcc 1
		.amdhsa_float_round_mode_32 0
		.amdhsa_float_round_mode_16_64 0
		.amdhsa_float_denorm_mode_32 3
		.amdhsa_float_denorm_mode_16_64 3
		.amdhsa_dx10_clamp 1
		.amdhsa_ieee_mode 1
		.amdhsa_fp16_overflow 0
		.amdhsa_tg_split 0
		.amdhsa_exception_fp_ieee_invalid_op 0
		.amdhsa_exception_fp_denorm_src 0
		.amdhsa_exception_fp_ieee_div_zero 0
		.amdhsa_exception_fp_ieee_overflow 0
		.amdhsa_exception_fp_ieee_underflow 0
		.amdhsa_exception_fp_ieee_inexact 0
		.amdhsa_exception_int_div_zero 0
	.end_amdhsa_kernel

; __global__ void __launch_bounds__(NTHR, 2) fwd(Args ka) {
.Lfunc_end0:
	.size	_Z3fwd4Args, .Lfunc_end0-_Z3fwd4Args
	.set _Z3fwd4Args.num_vgpr, 256
	.set _Z3fwd4Args.num_agpr, 0
	.set _Z3fwd4Args.numbered_sgpr, 98
	.set _Z3fwd4Args.num_named_barrier, 0
	.set _Z3fwd4Args.private_seg_size, 0
	.set _Z3fwd4Args.uses_vcc, 1
	.set _Z3fwd4Args.uses_flat_scratch, 0
	.set _Z3fwd4Args.has_dyn_sized_stack, 0
	.set _Z3fwd4Args.has_recursion, 0
	.set _Z3fwd4Args.has_indirect_call, 0

; #define LAS __attribute__((address_space(3)))
;     __device__ __forceinline__ const float* x() const { return (const float*)ld(0); }
;     __device__ __forceinline__ const float* c() const { return (const float*)ld(1); }
;     __device__ __forceinline__ const float* ctx() const { return (const float*)ld(2); }
; __global__ void __launch_bounds__(NTHR, 2) fwd(Args ka) {
;     extern __shared__ __attribute__((aligned(16))) unsigned char lds_raw[];
;     LAS unsigned char* lds = (LAS unsigned char*)lds_raw;
;     const int tid = threadIdx.x;
;     const int lo = ka.lo, hi = ka.hi;
;     for (int u = tid; u < 16; u += NTHR) ((LAS unsigned*)(lds + LDSCTL_OFF))[u] = 0u;
;     LAS unsigned long long* PTW = (LAS unsigned long long*)(lds + LDSCTL_OFF + 64);
;     if (tid == 0) {
;         PTW[0] = (unsigned long long)ka.x;
;         PTW[1] = (unsigned long long)ka.c;
;         PTW[2] = (unsigned long long)ka.ctx;
;         PTW[3] = (unsigned long long)ka.c_ctx;
;         PTW[4] = (unsigned long long)ka.w_mod;
;         PTW[5] = (unsigned long long)ka.b_mod;
;         PTW[6] = (unsigned long long)ka.g_mix;
;         PTW[7] = (unsigned long long)ka.g_ffn;
;         PTW[8] = (unsigned long long)ka.w_in;
;         PTW[9] = (unsigned long long)ka.w_out;
;         PTW[10] = (unsigned long long)ka.lq1;
;         PTW[11] = (unsigned long long)ka.lk1;
;         PTW[12] = (unsigned long long)ka.lq2;
;         PTW[13] = (unsigned long long)ka.lk2;
;         PTW[14] = (unsigned long long)ka.g_subln;
;         PTW[15] = (unsigned long long)ka.ln_g;
;         PTW[16] = (unsigned long long)ka.ln_b;
;         PTW[17] = (unsigned long long)ka.w_sp;
;         PTW[18] = (unsigned long long)ka.b_sp;
;         PTW[19] = (unsigned long long)ka.w_fo;
;         PTW[20] = (unsigned long long)ka.w_r;
;         PTW[21] = (unsigned long long)ka.w_gate;
;         PTW[22] = (unsigned long long)ka.w_up;
;         PTW[23] = (unsigned long long)ka.w_down;
;         PTW[24] = (unsigned long long)ka.g_final;
;         PTW[25] = (unsigned long long)ka.out; PTW[26] = (unsigned long long)ka.ws;
;     }
;     __syncthreads();
;     XcdBarrier bar; bar.bar = (unsigned*)(ka.ws + WS_CTL); bar.x = 0; bar.st = nullptr;
;     if (hi - lo > 1) bar = xcd_barrier_post((unsigned*)(ka.ws + WS_CTL), (volatile LAS unsigned*)(lds + LDSCTL_OFF));
amdhsa.kernels:
  - .agpr_count:     0
    .args:
      - .offset:         0
        .size:           224
        .value_kind:     by_value
      - .offset:         224
        .size:           4
        .value_kind:     hidden_block_count_x
      - .offset:         228
        .size:           4
        .value_kind:     hidden_block_count_y
      - .offset:         232
        .size:           4
        .value_kind:     hidden_block_count_z
      - .offset:         236
        .size:           2
        .value_kind:     hidden_group_size_x
      - .offset:         238
        .size:           2
        .value_kind:     hidden_group_size_y
      - .offset:         240
        .size:           2
        .value_kind:     hidden_group_size_z
      - .offset:         242
        .size:           2
        .value_kind:     hidden_remainder_x
      - .offset:         244
        .size:           2
        .value_kind:     hidden_remainder_y
      - .offset:         246
        .size:           2
        .value_kind:     hidden_remainder_z
      - .offset:         264
        .size:           8
        .value_kind:     hidden_global_offset_x
      - .offset:         272
        .size:           8
        .value_kind:     hidden_global_offset_y
      - .offset:         280
        .size:           8
        .value_kind:     hidden_global_offset_z
      - .offset:         288
        .size:           2
        .value_kind:     hidden_grid_dims
      - .offset:         344
        .size:           4
        .value_kind:     hidden_dynamic_lds_size
    .group_segment_fixed_size: 0
    .kernarg_segment_align: 8
    .kernarg_segment_size: 480
    .language:       OpenCL C
    .language_version:
      - 2
      - 0
    .max_flat_workgroup_size: 512
    .name:           _Z3fwd4Args
    .private_segment_fixed_size: 0
    .sgpr_count:     108
    .sgpr_spill_count: 25
    .symbol:         _Z3fwd4Args.kd
    .uniform_work_group_size: 1
    .uses_dynamic_stack: false
    .vgpr_count:     256
    .vgpr_spill_count: 0
    .wavefront_size: 64
